# quantizer ticket drawn one item ahead (pipelined draw, stop flag examined one item late, every drawn ticket processed) on top of P4/P8 latency edits
# speedup vs baseline: 1.0210x; 1.0101x over previous
; #define Q_LOAD() do { _Pragma("unroll") for (int g = 0; g < 8; ++g) _Pragma("unroll") for (int r = 0; r < 4; ++r) v[g][r] = __builtin_nontemporal_load((const f32x4*)(Wp + (size_t)(256 * g + 32 * wave + 4 * kr + r) * ldw + 4 * n4)); } while (0)
; #define Q_GRAB() (((stop != nullptr && xb_ld(stop) >= thr) || (quota > 0 && qleft-- <= 0)) ? (unsigned)hi : (unsigned)lo + atomicAdd(cnt, 1u))
;     ...
;     __syncthreads();
;     if (tid == 0) MISC[2] = Q_GRAB();
;     __syncthreads();
;     int cur = (int)MISC[2];
;     __syncthreads();
;     if (cur < hi) { Q_ITEM(cur); Q_LOAD(); }
.LBB0_309:
	v_mov_b32_e32 v199, 0x1800
	v_mov_b32_e32 v201, -1
	v_cmp_gt_u32_e32 vcc, 0x19c8, v1
	s_mov_b64 s[8:9], exec
	s_and_b64 exec, exec, vcc
	v_mov_b32_e32 v203, 1
	v_mov_b32_e32 v2, 0
	global_atomic_add v199, v2, v203, s[20:21] sc0
	global_load_dword v201, v2, s[22:23] sc1
	s_mov_b64 exec, s[8:9]
	s_add_i32 s3, 0, 0x27f08
	v_mov_b32_e32 v2, s3
	ds_write_b32 v2, v1

; #define LAS __attribute__((address_space(3)))
; #define Q_GRAB() (((stop != nullptr && xb_ld(stop) >= thr) || (quota > 0 && qleft-- <= 0)) ? (unsigned)hi : (unsigned)lo + atomicAdd(cnt, 1u))
;     ...
;         unsigned nxt = 0u; if (tid == 0) nxt = Q_GRAB();
;         signed char* Qc = Qp; float* csc = csp; const bool f8c = f8; const float qmax = f8c ? 448.0f : 127.0f, qinv = f8c ? (1.0f / 448.0f) : (1.0f / 127.0f);
;         f32x4 mx = {0.f, 0.f, 0.f, 0.f};
; #pragma unroll
;         for (int g = 0; g < 8; ++g)
; #pragma unroll
;             for (int r = 0; r < 4; ++r) { mx[0] = fmaxf(mx[0], fabsf(v[g][r][0])); mx[1] = fmaxf(mx[1], fabsf(v[g][r][1])); mx[2] = fmaxf(mx[2], fabsf(v[g][r][2])); mx[3] = fmaxf(mx[3], fabsf(v[g][r][3])); }
; #pragma unroll
;         for (int c = 0; c < 4; ++c) { float m = mx[c]; m = fmaxf(m, __shfl_xor(m, 8)); m = fmaxf(m, __shfl_xor(m, 16)); m = fmaxf(m, __shfl_xor(m, 32)); mx[c] = m; }
;         if (tid == 0) MISC[2] = nxt;
;         if (kr == 0) *(LAS f32x4*)(smax + wave * 32 + 4 * n4) = mx;
.LBB0_334:
	s_waitcnt vmcnt(10)
	v_max3_f32 v130, |v2|, 0, |v6|
	s_waitcnt vmcnt(8)
	v_max3_f32 v130, v130, |v10|, |v14|
	v_max3_f32 v130, v130, |v18|, |v22|
	v_max3_f32 v130, v130, |v26|, |v30|
	v_max3_f32 v130, v130, |v34|, |v38|
	v_max3_f32 v130, v130, |v42|, |v46|
	v_max3_f32 v131, |v3|, 0, |v7|
	v_max3_f32 v130, v130, |v50|, |v54|
	v_max3_f32 v132, |v4|, 0, |v8|
	v_max3_f32 v131, v131, |v11|, |v15|
	v_max3_f32 v130, v130, |v58|, |v62|
	v_max3_f32 v132, v132, |v12|, |v16|
	v_max3_f32 v131, v131, |v19|, |v23|
	v_max3_f32 v130, v130, |v66|, |v70|
	v_max3_f32 v132, v132, |v20|, |v24|
	v_max3_f32 v131, v131, |v27|, |v31|
	v_max3_f32 v130, v130, |v74|, |v78|
	v_max3_f32 v132, v132, |v28|, |v32|
	v_max3_f32 v131, v131, |v35|, |v39|
	v_max3_f32 v130, v130, |v82|, |v86|
	v_max3_f32 v132, v132, |v36|, |v40|
	v_max3_f32 v131, v131, |v43|, |v47|
	v_max3_f32 v130, v130, |v90|, |v94|
	v_max3_f32 v132, v132, |v44|, |v48|
	v_max3_f32 v131, v131, |v51|, |v55|
	s_waitcnt vmcnt(6)
	v_max3_f32 v130, v130, |v98|, |v102|
	v_max3_f32 v133, |v5|, 0, |v9|
	v_max3_f32 v132, v132, |v52|, |v56|
	v_max3_f32 v131, v131, |v59|, |v63|
	s_waitcnt vmcnt(4)
	v_max3_f32 v130, v130, |v106|, |v110|
	v_max3_f32 v133, v133, |v13|, |v17|
	v_max3_f32 v132, v132, |v60|, |v64|
	v_max3_f32 v131, v131, |v67|, |v71|
	s_waitcnt vmcnt(2)
	v_max3_f32 v130, v130, |v114|, |v118|
	v_max3_f32 v133, v133, |v21|, |v25|
	v_max3_f32 v132, v132, |v68|, |v72|
	v_max3_f32 v131, v131, |v75|, |v79|
	s_waitcnt vmcnt(0)
	v_max3_f32 v130, v130, |v122|, |v126|
	v_max3_f32 v133, v133, |v29|, |v33|
	v_max3_f32 v132, v132, |v76|, |v80|
	v_max3_f32 v131, v131, |v83|, |v87|
	ds_bpermute_b32 v134, v163, v130
	v_max3_f32 v133, v133, |v37|, |v41|
	v_max3_f32 v132, v132, |v84|, |v88|
	v_max3_f32 v131, v131, |v91|, |v95|
	v_max3_f32 v133, v133, |v45|, |v49|
	v_max3_f32 v132, v132, |v92|, |v96|
	v_max3_f32 v131, v131, |v99|, |v103|
	v_max3_f32 v133, v133, |v53|, |v57|
	v_max3_f32 v132, v132, |v100|, |v104|
	v_max3_f32 v131, v131, |v107|, |v111|
	v_max3_f32 v133, v133, |v61|, |v65|
	v_max3_f32 v132, v132, |v108|, |v112|
	v_max3_f32 v131, v131, |v115|, |v119|
	v_max3_f32 v133, v133, |v69|, |v73|
	v_max3_f32 v132, v132, |v116|, |v120|
	v_max3_f32 v131, v131, |v123|, |v127|
	s_waitcnt lgkmcnt(0)
	v_max_f32_e32 v134, v134, v134
	v_max3_f32 v133, v133, |v77|, |v81|
	v_max3_f32 v135, v132, |v124|, |v128|
	ds_bpermute_b32 v132, v163, v131
	v_max_f32_e32 v130, v130, v134
	v_max3_f32 v133, v133, |v85|, |v89|
	ds_bpermute_b32 v134, v165, v130
	v_max3_f32 v133, v133, |v93|, |v97|
	v_max3_f32 v133, v133, |v101|, |v105|
	v_max3_f32 v133, v133, |v109|, |v113|
	v_max3_f32 v133, v133, |v117|, |v121|
	s_waitcnt lgkmcnt(1)
	v_max_f32_e32 v132, v132, v132
	v_max3_f32 v133, v133, |v125|, |v129|
	v_max_f32_e32 v132, v131, v132
	s_waitcnt lgkmcnt(0)
	v_max_f32_e32 v131, v134, v134
	ds_bpermute_b32 v134, v163, v135
	ds_bpermute_b32 v136, v165, v132
	ds_bpermute_b32 v137, v163, v133
	v_max_f32_e32 v130, v130, v131
	ds_bpermute_b32 v131, v167, v130
	s_waitcnt lgkmcnt(3)
	v_max_f32_e32 v134, v134, v134
	s_waitcnt lgkmcnt(2)
	v_max_f32_e32 v136, v136, v136
	v_max_f32_e32 v134, v135, v134
	s_waitcnt lgkmcnt(1)
	v_max_f32_e32 v135, v137, v137
	v_max_f32_e32 v132, v132, v136
	ds_bpermute_b32 v136, v165, v134
	v_max_f32_e32 v137, v133, v135
	ds_bpermute_b32 v138, v165, v137
	ds_bpermute_b32 v135, v167, v132
	s_waitcnt lgkmcnt(2)
	v_max_f32_e32 v133, v136, v136
	v_max_f32_e32 v133, v134, v133
	s_waitcnt lgkmcnt(1)
	v_max_f32_e32 v134, v138, v138
	v_max_f32_e32 v134, v137, v134
	ds_bpermute_b32 v136, v167, v133
	ds_bpermute_b32 v137, v167, v134
	s_and_saveexec_b64 s[6:7], s[40:41]
	v_add_u32_e32 v1, 0x1c8, v199
	v_cmp_lt_u32_e32 vcc, 23, v201
	s_mov_b64 s[12:13], vcc
	v_cmp_le_u32_e32 vcc, 0x19c8, v1
	s_or_b64 s[12:13], s[12:13], vcc
	v_mov_b32_e32 v199, 0x1800
	s_andn2_b64 exec, exec, s[12:13]
	v_mov_b32_e32 v203, 1
	global_atomic_add v199, v171, v203, s[20:21] sc0
	s_and_b64 exec, s[6:7], s[40:41]
	global_load_dword v201, v171, s[22:23] sc1
	v_mov_b32_e32 v138, s75
	ds_write_b32 v138, v1
	s_or_b64 exec, exec, s[6:7]
	s_and_saveexec_b64 s[6:7], s[4:5]
	s_cbranch_execz .LBB0_343
	v_max_f32_e32 v1, v131, v131
	v_max_f32_e32 v130, v130, v130
	v_max_f32_e32 v130, v130, v1
	s_waitcnt lgkmcnt(2)
	v_max_f32_e32 v1, v135, v135
	v_max_f32_e32 v131, v132, v132
	v_max_f32_e32 v131, v131, v1
	s_waitcnt lgkmcnt(1)
	v_max_f32_e32 v1, v136, v136
	v_max_f32_e32 v132, v133, v133
	v_max_f32_e32 v132, v132, v1
	s_waitcnt lgkmcnt(0)
	v_max_f32_e32 v1, v137, v137
	v_max_f32_e32 v133, v134, v134
	v_max_f32_e32 v133, v133, v1
	v_add_u32_e32 v1, s44, v169
	ds_write_b128 v1, v[130:133]

; DI void attn_unit(LAS unsigned char* ldsb, const bf16* proj, const bf16* KR, const bf16* VTg, const float* rope, const float* sinks, unsigned char* yab, int kvh, int ab) {
;     ...
;         const int Tn = Tq + 9; const bool pre = (qt < 3) && Tn >= 0 && Tn < NTOK / 32; u32x4 nk = {0u, 0u, 0u, 0u};
;         if (pre) { if (tid < 256) nk = *(const u32x4*)(KR + ((size_t)(kvh * MROWS + Tn * 32 + (tid >> 3))) * 64 + (tid & 7) * 8);
;                    else { const int t2 = tid - 256; nk = *(const u32x4*)(VTg + ((size_t)(kvh * 64 + (t2 >> 2))) * MROWS + Tn * 32 + (t2 & 3) * 8); } }
;         if (qt < 3) AT_LOADQ(p0 + 32);
.LBB0_1301:
	s_waitcnt vmcnt(3)
	v_mov_b32_e32 v56, v12
	v_mov_b32_e32 v57, v13
	v_mov_b32_e32 v58, v14
	v_mov_b32_e32 v59, v15
	s_waitcnt vmcnt(2)
	v_mov_b32_e32 v60, v4
	v_mov_b32_e32 v61, v5
	v_mov_b32_e32 v62, v6
	v_mov_b32_e32 v63, v7
	s_waitcnt vmcnt(1)
	v_mov_b32_e32 v64, v16
	v_mov_b32_e32 v65, v17
	v_mov_b32_e32 v66, v18
	v_mov_b32_e32 v67, v19
	s_waitcnt vmcnt(0)
	v_mov_b32_e32 v68, v8
	v_mov_b32_e32 v69, v9
	v_mov_b32_e32 v70, v10
	v_mov_b32_e32 v71, v11
	s_or_b32 s68, s67, s66
	s_cmp_lg_u32 s67, 3
	s_cselect_b64 s[4:5], -1, 0
	s_cmpk_lt_u32 s68, 0x1fb
	s_cselect_b64 s[6:7], -1, 0
	v_mov_b32_e32 v52, 0
	s_and_b64 s[42:43], s[4:5], s[6:7]
	s_andn2_b64 vcc, exec, s[42:43]
	v_mov_b32_e32 v53, v52
	v_mov_b32_e32 v54, v52
	v_mov_b32_e32 v55, v52
	s_cbranch_vccnz .LBB0_1307
	s_lshl_b32 s8, s68, 5
	s_and_saveexec_b64 s[6:7], s[26:27]
	s_xor_b64 s[6:7], exec, s[6:7]
	s_cbranch_execz .LBB0_1304
	s_lshl_b32 s24, s8, 1
	v_lshl_add_u64 v[52:53], v[116:117], 0, s[24:25]
	global_load_dwordx4 v[52:55], v[52:53], off offset:320

; DI float bflo(unsigned w) { return __uint_as_float(w << 16); }
; DI float bfhi(unsigned w) { return __uint_as_float(w & 0xffff0000u); }
; DI void attn_unit(LAS unsigned char* ldsb, const bf16* proj, const bf16* KR, const bf16* VTg, const float* rope, const float* sinks, unsigned char* yab, int kvh, int ab) {
;     ...
;     AT_LOADQ(ab * 128);
;     __syncthreads();
;     for (int qt = 0; qt < 4; ++qt) {
;         const int p0 = ab * 128 + 32 * qt, kb0 = p0 - 128, qp = p0 + r, Tq = ab * 4 + qt - 4;
;         bf16x8 qf[4];
; #pragma unroll
;         for (int ks = 0; ks < 2; ++ks) { float o1[8], o2[8];
; #pragma unroll
;             for (int q = 0; q < 4; ++q) {
;                 const float a0 = bflo(raw[ks][q]), a1 = bfhi(raw[ks][q]), b0 = bflo(raw[ks + 2][q]), b1 = bfhi(raw[ks + 2][q]);
;                 o1[2 * q] = a0 * cs[ks][2 * q] - b0 * sn[ks][2 * q]; o2[2 * q] = b0 * cs[ks][2 * q] + a0 * sn[ks][2 * q];
;                 o1[2 * q + 1] = a1 * cs[ks][2 * q + 1] - b1 * sn[ks][2 * q + 1]; o2[2 * q + 1] = b1 * cs[ks][2 * q + 1] + a1 * sn[ks][2 * q + 1]; }
;             qf[ks] = pack8(o1[0], o1[1], o1[2], o1[3], o1[4], o1[5], o1[6], o1[7]);
;             qf[ks + 2] = pack8(o2[0], o2[1], o2[2], o2[3], o2[4], o2[5], o2[6], o2[7]); }
;         const int Tn = Tq + 9; const bool pre = (qt < 3) && Tn >= 0 && Tn < NTOK / 32; u32x4 nk = {0u, 0u, 0u, 0u};
;         if (pre) { if (tid < 256) nk = *(const u32x4*)(KR + ((size_t)(kvh * MROWS + Tn * 32 + (tid >> 3))) * 64 + (tid & 7) * 8);
;                    else { const int t2 = tid - 256; nk = *(const u32x4*)(VTg + ((size_t)(kvh * 64 + (t2 >> 2))) * MROWS + Tn * 32 + (t2 & 3) * 8); } }
;         if (qt < 3) AT_LOADQ(p0 + 32);
.LBB0_1307:
	s_lshl_b32 s69, s67, 5
	s_add_i32 s69, s69, s34
	s_andn2_b64 vcc, exec, s[4:5]
	v_mov_b64_e32 v[140:141], v[22:23]
	v_mov_b64_e32 v[136:137], v[28:29]
	v_mov_b64_e32 v[132:133], v[36:37]
	v_mov_b64_e32 v[128:129], v[38:39]
	v_mov_b64_e32 v[124:125], v[42:43]
	v_mov_b64_e32 v[120:121], v[46:47]
	v_mov_b64_e32 v[150:151], v[20:21]
	v_mov_b64_e32 v[146:147], v[24:25]
	v_mov_b64_e32 v[142:143], v[32:33]
	v_mov_b64_e32 v[138:139], v[34:35]
	v_mov_b64_e32 v[134:135], v[40:41]
	v_mov_b64_e32 v[130:131], v[44:45]
	v_mov_b64_e32 v[126:127], v[48:49]
	v_mov_b64_e32 v[122:123], v[50:51]
	v_mov_b64_e32 v[144:145], v[30:31]
	v_mov_b64_e32 v[148:149], v[26:27]
	s_cbranch_vccnz .LBB0_1309
	s_add_i32 s4, s69, 32
	v_or_b32_e32 v56, s4, v1
	v_mov_b32_e32 v57, v2
	s_and_b32 s24, s4, 0x7fc0
	v_lshl_add_u64 v[58:59], v[96:97], 0, s[24:25]
	v_lshlrev_b32_e32 v3, 6, v56
	v_lshl_add_u64 v[56:57], s[36:37], 0, v[56:57]
	v_lshl_add_u64 v[60:61], v[98:99], 0, s[24:25]
	global_load_dwordx4 v[72:75], v[58:59], off offset:16
	global_load_dwordx4 v[76:79], v[58:59], off
	global_load_dwordx4 v[80:83], v[60:61], off offset:16
	global_load_dwordx4 v[84:87], v[60:61], off
	v_and_b32_e32 v58, 0xfc0, v3
	v_mov_b32_e32 v59, v2
	v_lshlrev_b64 v[56:57], 7, v[56:57]
	v_lshl_add_u64 v[60:61], v[104:105], 0, v[58:59]
	v_lshl_add_u64 v[58:59], v[106:107], 0, v[58:59]
	v_lshl_add_u64 v[68:69], v[94:95], 0, v[56:57]
	global_load_dwordx4 v[146:149], v[60:61], off offset:16
	global_load_dwordx4 v[138:141], v[60:61], off
	global_load_dwordx4 v[176:179], v[58:59], off offset:16
	global_load_dwordx4 v[142:145], v[58:59], off
	s_nop 0
	global_load_dwordx4 v[56:59], v[68:69], off
	global_load_dwordx4 v[60:63], v[68:69], off offset:32
	global_load_dwordx4 v[64:67], v[68:69], off offset:64
	s_nop 0
	global_load_dwordx4 v[68:71], v[68:69], off offset:96
	s_waitcnt vmcnt(11)
	v_pk_mul_f32 v[128:129], v[72:73], s[30:31] op_sel_hi:[1,0]
	s_waitcnt vmcnt(10)
	v_pk_mul_f32 v[120:121], v[76:77], s[30:31] op_sel_hi:[1,0]
	v_pk_mul_f32 v[124:125], v[78:79], s[30:31] op_sel_hi:[1,0]
	s_waitcnt vmcnt(8)
	v_pk_mul_f32 v[122:123], v[84:85], s[30:31] op_sel_hi:[1,0]
	v_pk_mul_f32 v[126:127], v[86:87], s[30:31] op_sel_hi:[1,0]
	v_pk_mul_f32 v[130:131], v[80:81], s[30:31] op_sel_hi:[1,0]
	v_pk_mul_f32 v[132:133], v[74:75], s[30:31] op_sel_hi:[1,0]
	v_pk_mul_f32 v[134:135], v[82:83], s[30:31] op_sel_hi:[1,0]
	s_waitcnt vmcnt(6)
	v_pk_mul_f32 v[136:137], v[138:139], s[30:31] op_sel_hi:[1,0]
	v_pk_mul_f32 v[140:141], v[140:141], s[30:31] op_sel_hi:[1,0]
	s_waitcnt vmcnt(4)
	v_pk_mul_f32 v[138:139], v[142:143], s[30:31] op_sel_hi:[1,0]
	v_pk_mul_f32 v[142:143], v[144:145], s[30:31] op_sel_hi:[1,0]
	v_pk_mul_f32 v[144:145], v[146:147], s[30:31] op_sel_hi:[1,0]
	v_pk_mul_f32 v[146:147], v[176:177], s[30:31] op_sel_hi:[1,0]
	v_pk_mul_f32 v[148:149], v[148:149], s[30:31] op_sel_hi:[1,0]
	v_pk_mul_f32 v[150:151], v[178:179], s[30:31] op_sel_hi:[1,0]
; DI float bflo(unsigned w) { return __uint_as_float(w << 16); }
; DI float bfhi(unsigned w) { return __uint_as_float(w & 0xffff0000u); }
; DI void attn_unit(LAS unsigned char* ldsb, const bf16* proj, const bf16* KR, const bf16* VTg, const float* rope, const float* sinks, unsigned char* yab, int kvh, int ab) {
;     ...
; #pragma unroll
;         for (int ks = 0; ks < 2; ++ks) { float o1[8], o2[8];
; #pragma unroll
;             for (int q = 0; q < 4; ++q) {
;                 const float a0 = bflo(raw[ks][q]), a1 = bfhi(raw[ks][q]), b0 = bflo(raw[ks + 2][q]), b1 = bfhi(raw[ks + 2][q]);
;                 o1[2 * q] = a0 * cs[ks][2 * q] - b0 * sn[ks][2 * q]; o2[2 * q] = b0 * cs[ks][2 * q] + a0 * sn[ks][2 * q];
;                 o1[2 * q + 1] = a1 * cs[ks][2 * q + 1] - b1 * sn[ks][2 * q + 1]; o2[2 * q + 1] = b1 * cs[ks][2 * q + 1] + a1 * sn[ks][2 * q + 1]; }
;             qf[ks] = pack8(o1[0], o1[1], o1[2], o1[3], o1[4], o1[5], o1[6], o1[7]);
;             qf[ks + 2] = pack8(o2[0], o2[1], o2[2], o2[3], o2[4], o2[5], o2[6], o2[7]); }
;         const int Tn = Tq + 9; const bool pre = (qt < 3) && Tn >= 0 && Tn < NTOK / 32; u32x4 nk = {0u, 0u, 0u, 0u};
;         if (pre) { if (tid < 256) nk = *(const u32x4*)(KR + ((size_t)(kvh * MROWS + Tn * 32 + (tid >> 3))) * 64 + (tid & 7) * 8);
;                    else { const int t2 = tid - 256; nk = *(const u32x4*)(VTg + ((size_t)(kvh * 64 + (t2 >> 2))) * MROWS + Tn * 32 + (t2 & 3) * 8); } }
;         if (qt < 3) AT_LOADQ(p0 + 32);
;         float m_run = sinks[head] * 1.4426950408889634f, l_run = h5 ? 0.f : 1.f;
;         f32x16 o0, o1;
; #pragma unroll
;         for (int i = 0; i < 16; ++i) { o0[i] = 0.f; o1[i] = 0.f; }
.LBB0_1309:
	s_load_dword s8, s[38:39], 0x0
	v_lshlrev_b32_e32 v72, 16, v12
	v_and_b32_e32 v73, 0xffff0000, v12
	v_lshlrev_b32_e32 v74, 16, v16
	v_and_b32_e32 v75, 0xffff0000, v16
	v_pk_mul_f32 v[76:77], v[50:51], v[72:73]
	v_pk_mul_f32 v[50:51], v[50:51], v[74:75]
	v_lshlrev_b32_e32 v12, 16, v13
	v_and_b32_e32 v13, 0xffff0000, v13
	v_pk_fma_f32 v[76:77], v[46:47], v[74:75], v[76:77]
	v_pk_fma_f32 v[46:47], v[46:47], v[72:73], v[50:51] neg_lo:[0,0,1] neg_hi:[0,0,1]
	v_lshlrev_b32_e32 v16, 16, v17
	v_and_b32_e32 v17, 0xffff0000, v17
	v_pk_mul_f32 v[50:51], v[48:49], v[12:13]
	v_cvt_pk_bf16_f32 v72, v46, v47
	v_pk_fma_f32 v[50:51], v[42:43], v[16:17], v[50:51]
	v_pk_mul_f32 v[16:17], v[48:49], v[16:17]
	v_cvt_pk_bf16_f32 v76, v76, v77
	v_pk_fma_f32 v[12:13], v[42:43], v[12:13], v[16:17] neg_lo:[0,0,1] neg_hi:[0,0,1]
	v_lshlrev_b32_e32 v16, 16, v14
	v_and_b32_e32 v17, 0xffff0000, v14
	v_lshlrev_b32_e32 v42, 16, v18
	v_and_b32_e32 v43, 0xffff0000, v18
	v_pk_mul_f32 v[48:49], v[44:45], v[16:17]
	v_lshlrev_b32_e32 v14, 16, v15
	v_pk_fma_f32 v[48:49], v[38:39], v[42:43], v[48:49]
	v_pk_mul_f32 v[42:43], v[44:45], v[42:43]
	v_and_b32_e32 v15, 0xffff0000, v15
	v_pk_fma_f32 v[16:17], v[38:39], v[16:17], v[42:43] neg_lo:[0,0,1] neg_hi:[0,0,1]
	v_lshlrev_b32_e32 v18, 16, v19
	v_and_b32_e32 v19, 0xffff0000, v19
	v_pk_mul_f32 v[38:39], v[40:41], v[14:15]
	v_cvt_pk_bf16_f32 v73, v12, v13
	v_pk_fma_f32 v[38:39], v[36:37], v[18:19], v[38:39]
	v_pk_mul_f32 v[18:19], v[40:41], v[18:19]
	v_lshlrev_b32_e32 v12, 16, v4
	v_pk_fma_f32 v[14:15], v[36:37], v[14:15], v[18:19] neg_lo:[0,0,1] neg_hi:[0,0,1]
	v_and_b32_e32 v13, 0xffff0000, v4
	v_cvt_pk_bf16_f32 v74, v16, v17
	v_cvt_pk_bf16_f32 v75, v14, v15
	v_lshlrev_b32_e32 v14, 16, v8
	v_and_b32_e32 v15, 0xffff0000, v8
	v_pk_mul_f32 v[16:17], v[34:35], v[12:13]
	v_lshlrev_b32_e32 v4, 16, v5
	v_pk_fma_f32 v[16:17], v[28:29], v[14:15], v[16:17]
	v_pk_mul_f32 v[14:15], v[34:35], v[14:15]
	v_and_b32_e32 v5, 0xffff0000, v5
	v_pk_fma_f32 v[12:13], v[28:29], v[12:13], v[14:15] neg_lo:[0,0,1] neg_hi:[0,0,1]
	v_lshlrev_b32_e32 v8, 16, v9
	v_and_b32_e32 v9, 0xffff0000, v9
	v_pk_mul_f32 v[14:15], v[32:33], v[4:5]
	v_lshlrev_b32_e32 v18, 16, v10
	v_pk_fma_f32 v[14:15], v[22:23], v[8:9], v[14:15]
	v_pk_mul_f32 v[8:9], v[32:33], v[8:9]
	v_and_b32_e32 v19, 0xffff0000, v10
	v_pk_fma_f32 v[4:5], v[22:23], v[4:5], v[8:9] neg_lo:[0,0,1] neg_hi:[0,0,1]
	v_lshlrev_b32_e32 v8, 16, v6
	v_and_b32_e32 v9, 0xffff0000, v6
	v_pk_mul_f32 v[22:23], v[24:25], v[8:9]
	v_lshlrev_b32_e32 v6, 16, v7
	v_pk_fma_f32 v[22:23], v[30:31], v[18:19], v[22:23]
	v_pk_mul_f32 v[18:19], v[24:25], v[18:19]
	v_and_b32_e32 v7, 0xffff0000, v7
	v_pk_fma_f32 v[8:9], v[30:31], v[8:9], v[18:19] neg_lo:[0,0,1] neg_hi:[0,0,1]
	v_lshlrev_b32_e32 v10, 16, v11
	v_and_b32_e32 v11, 0xffff0000, v11
	v_pk_mul_f32 v[18:19], v[20:21], v[6:7]
	v_cvt_pk_bf16_f32 v84, v16, v17
	v_pk_fma_f32 v[18:19], v[26:27], v[10:11], v[18:19]
	v_pk_mul_f32 v[10:11], v[20:21], v[10:11]
	v_mov_b32_e32 v16, v2
	v_pk_fma_f32 v[6:7], v[26:27], v[6:7], v[10:11] neg_lo:[0,0,1] neg_hi:[0,0,1]
	v_mov_b32_e32 v17, v2
	v_cvt_pk_bf16_f32 v80, v12, v13
	v_cvt_pk_bf16_f32 v81, v4, v5
	v_cvt_pk_bf16_f32 v82, v8, v9
	v_cvt_pk_bf16_f32 v83, v6, v7
	v_cvt_pk_bf16_f32 v85, v14, v15
	v_cvt_pk_bf16_f32 v86, v22, v23
	v_mov_b32_e32 v4, v2
	s_waitcnt lgkmcnt(0)
	v_mov_b32_e32 v3, s8
	v_mul_f32_e32 v178, 0x3fb8aa3b, v3
	v_mov_b32_e32 v3, v2
	v_mov_b32_e32 v5, v2
	v_mov_b32_e32 v6, v2
	v_mov_b32_e32 v7, v2
	v_mov_b32_e32 v8, v2
	v_mov_b32_e32 v9, v2
	v_mov_b32_e32 v10, v2
	v_mov_b32_e32 v11, v2
	v_mov_b32_e32 v12, v2
	v_mov_b32_e32 v13, v2
	v_mov_b32_e32 v14, v2
	v_mov_b32_e32 v15, v2
	v_mov_b64_e32 v[34:35], v[16:17]
	v_cvt_pk_bf16_f32 v87, v18, v19
	v_mov_b64_e32 v[32:33], v[14:15]
	v_mov_b64_e32 v[30:31], v[12:13]
	v_mov_b64_e32 v[28:29], v[10:11]
	v_mov_b64_e32 v[26:27], v[8:9]
	v_mov_b64_e32 v[24:25], v[6:7]
	v_mov_b64_e32 v[22:23], v[4:5]
	v_mov_b64_e32 v[20:21], v[2:3]
	v_mov_b64_e32 v[18:19], v[16:17]
	v_cvt_pk_bf16_f32 v77, v50, v51
	v_cvt_pk_bf16_f32 v78, v48, v49
	v_cvt_pk_bf16_f32 v79, v38, v39
	s_mov_b32 s24, 0
	s_mov_b32 s54, s35
	v_mov_b32_e32 v176, v173
	v_mov_b32_e32 v177, v168
	v_mov_b32_e32 v175, v93
	v_mov_b64_e32 v[16:17], v[14:15]
	v_mov_b64_e32 v[14:15], v[12:13]
	v_mov_b64_e32 v[12:13], v[10:11]
	v_mov_b64_e32 v[10:11], v[8:9]
	v_mov_b64_e32 v[8:9], v[6:7]
	v_mov_b64_e32 v[6:7], v[4:5]
	v_mov_b64_e32 v[4:5], v[2:3]
	s_mov_b32 s55, 0
	s_branch .LBB0_1312

; #define LAS __attribute__((address_space(3)))
; DI void attn_unit(LAS unsigned char* ldsb, const bf16* proj, const bf16* KR, const bf16* VTg, const float* rope, const float* sinks, unsigned char* yab, int kvh, int ab) {
;     ...
;         const float l = l_run + __shfl_xor(l_run, 32), inv = 1.0f / l;
;         unsigned char* orow = yab + (size_t)qp * D + head * 64 + 4 * h5;
; #pragma unroll
;         for (int g4 = 0; g4 < 4; ++g4) {
;             int a = __builtin_amdgcn_cvt_pk_fp8_f32(o0[4 * g4] * inv, o0[4 * g4 + 1] * inv, 0, false); a = __builtin_amdgcn_cvt_pk_fp8_f32(o0[4 * g4 + 2] * inv, o0[4 * g4 + 3] * inv, a, true); *(int*)(orow + 8 * g4) = a;
;             int b = __builtin_amdgcn_cvt_pk_fp8_f32(o1[4 * g4] * inv, o1[4 * g4 + 1] * inv, 0, false); b = __builtin_amdgcn_cvt_pk_fp8_f32(o1[4 * g4 + 2] * inv, o1[4 * g4 + 3] * inv, b, true); *(int*)(orow + 32 + 8 * g4) = b;
;         }
;         if (pre) { const int slot = (Tn + 2 * NSLOT) % NSLOT;
;             if (tid < 256) *(LAS u32x4*)(KL + (slot * 32 + (tid >> 3)) * KRS + (tid & 7) * 16) = nk;
;             else { const int t2 = tid - 256; u32x2 a; a.x = nk.x; a.y = nk.y; u32x2 b; b.x = nk.z; b.y = nk.w; LAS unsigned char* dst = VL + (t2 >> 2) * VLRS + slot * 64 + (t2 & 3) * 16; *(LAS u32x2*)dst = a; *(LAS u32x2*)(dst + 8) = b; } }
;         __syncthreads();
.LBB0_1315:
	s_waitcnt vmcnt(0)
	ds_bpermute_b32 v3, v155, v175
	v_or_b32_e32 v36, s69, v1
	v_mov_b32_e32 v37, v2
	v_lshlrev_b32_e32 v36, 11, v36
	v_lshl_add_u64 v[36:37], v[118:119], 0, v[36:37]
	s_waitcnt lgkmcnt(0)
	v_add_f32_e32 v3, v175, v3
	v_div_scale_f32 v38, s[4:5], v3, v3, 1.0
	v_rcp_f32_e32 v39, v38
	v_div_scale_f32 v40, vcc, 1.0, v3, 1.0
	v_fma_f32 v41, -v38, v39, 1.0
	v_fmac_f32_e32 v39, v41, v39
	v_mul_f32_e32 v41, v40, v39
	v_fma_f32 v42, -v38, v41, v40
	v_fmac_f32_e32 v41, v42, v39
	v_fma_f32 v38, -v38, v41, v40
	v_div_fmas_f32 v38, v38, v39, v41
	v_div_fixup_f32 v3, v38, v3, 1.0
	v_mul_f32_e32 v20, v20, v3
	v_mul_f32_e32 v21, v21, v3
	v_mov_b32_e32 v38, v2
	v_cvt_pk_fp8_f32 v38, v20, v21
	v_mul_f32_e32 v20, v22, v3
	v_mul_f32_e32 v4, v4, v3
	v_mul_f32_e32 v5, v5, v3
	v_mov_b32_e32 v22, v2
	v_cvt_pk_fp8_f32 v22, v4, v5
	v_mul_f32_e32 v4, v6, v3
	v_mul_f32_e32 v5, v7, v3
	v_mov_b32_e32 v6, v2
	v_cvt_pk_fp8_f32 v22, v4, v5 op_sel:[0,0,1]
	v_mul_f32_e32 v4, v24, v3
	v_mul_f32_e32 v5, v25, v3
	v_cvt_pk_fp8_f32 v6, v4, v5
	v_mul_f32_e32 v7, v8, v3
	v_mul_f32_e32 v8, v9, v3
	v_mov_b32_e32 v9, v2
	v_mul_f32_e32 v21, v23, v3
	v_cvt_pk_fp8_f32 v9, v7, v8
	v_cvt_pk_fp8_f32 v38, v20, v21 op_sel:[0,0,1]
	v_mul_f32_e32 v4, v26, v3
	v_mul_f32_e32 v5, v27, v3
	v_cvt_pk_fp8_f32 v6, v4, v5 op_sel:[0,0,1]
	v_mul_f32_e32 v4, v10, v3
	v_mul_f32_e32 v5, v11, v3
	v_cvt_pk_fp8_f32 v9, v4, v5 op_sel:[0,0,1]
	global_store_dword v[36:37], v38, off
	global_store_dword v[36:37], v22, off offset:32
	global_store_dword v[36:37], v6, off offset:8
	global_store_dword v[36:37], v9, off offset:40
	v_mul_f32_e32 v4, v28, v3
	v_mul_f32_e32 v5, v29, v3
	v_mov_b32_e32 v6, v2
	v_cvt_pk_fp8_f32 v6, v4, v5
	v_mul_f32_e32 v7, v12, v3
	v_mul_f32_e32 v8, v13, v3
	v_mov_b32_e32 v9, v2
	v_cvt_pk_fp8_f32 v9, v7, v8
	v_mul_f32_e32 v4, v30, v3
	v_mul_f32_e32 v5, v31, v3
	v_cvt_pk_fp8_f32 v6, v4, v5 op_sel:[0,0,1]
	v_mul_f32_e32 v4, v14, v3
	v_mul_f32_e32 v5, v15, v3
	v_cvt_pk_fp8_f32 v9, v4, v5 op_sel:[0,0,1]
	v_mul_f32_e32 v4, v32, v3
	v_mul_f32_e32 v5, v33, v3
	v_mov_b32_e32 v7, v2
	v_cvt_pk_fp8_f32 v7, v4, v5
	v_mul_f32_e32 v8, v16, v3
	v_mul_f32_e32 v10, v17, v3
	v_mov_b32_e32 v11, v2
	v_cvt_pk_fp8_f32 v11, v8, v10
	v_mul_f32_e32 v4, v34, v3
	v_mul_f32_e32 v5, v35, v3
	v_cvt_pk_fp8_f32 v7, v4, v5 op_sel:[0,0,1]
	v_mul_f32_e32 v4, v18, v3
	v_mul_f32_e32 v3, v19, v3
	v_cvt_pk_fp8_f32 v11, v4, v3 op_sel:[0,0,1]
	s_and_b64 vcc, exec, s[42:43]
	global_store_dword v[36:37], v6, off offset:16
	global_store_dword v[36:37], v9, off offset:48
	global_store_dword v[36:37], v7, off offset:24
	global_store_dword v[36:37], v11, off offset:56
	s_cbranch_vccz .LBB0_1300
	s_add_i32 s68, s68, 25
	s_and_b32 s4, s68, 0xffff
	s_mul_i32 s4, s4, 0xcccd
	s_lshr_b32 s4, s4, 19
	s_mul_i32 s4, s4, 10
	s_sub_i32 s4, s68, s4
	s_and_b32 s6, s4, 0xffff
	s_and_saveexec_b64 s[4:5], s[26:27]
	s_xor_b64 s[4:5], exec, s[4:5]
	v_lshl_add_u32 v3, s6, 6, v157
	ds_write2_b64 v3, v[52:53], v[54:55] offset1:1
	s_andn2_saveexec_b64 s[4:5], s[4:5]
	s_cbranch_execz .LBB0_1299
	v_lshl_or_b32 v3, s6, 5, v89
	v_mad_u32_u24 v3, v3, s45, v158
	ds_write_b128 v3, v[52:55]
	s_branch .LBB0_1299

; __global__ void __launch_bounds__(NWAVES * 64, 2) fwd_kernel(Args a_unused) {
;     ...
;                 const float qi = 127.0f / am;
;                 if (lane == 0) ((float*)(ws + WS_CS + CS_ROW))[m] = am * (1.0f / 127.0f);
;                 unsigned* hq = (unsigned*)((signed char*)(ws + WS_H) + (size_t)m * D + 4 * lane);
; #pragma unroll
;                 for (int j = 0; j < 8; ++j) hq[64 * j] = q8x4(v[j][0], v[j][1], v[j][2], v[j][3], qi); }
;             f32x4 acc0 = {0.f, 0.f, 0.f, 0.f}, acc1 = {0.f, 0.f, 0.f, 0.f};
;             const unsigned short* xa = X1 + (size_t)(row0 + r16) * D + 256 * wave + 8 * kk;
; #pragma unroll
;             for (int sK = 0; sK < 8; ++sK) { const bf16x8 af = __builtin_bit_cast(bf16x8, *(const u32x4*)(xa + 32 * sK));
;                 acc0 = __builtin_amdgcn_mfma_f32_16x16x32_bf16(af, bh[sK][0], acc0, 0, 0, 0); acc0 = __builtin_amdgcn_mfma_f32_16x16x32_bf16(af, bl[sK][0], acc0, 0, 0, 0);
;                 acc1 = __builtin_amdgcn_mfma_f32_16x16x32_bf16(af, bh[sK][1], acc1, 0, 0, 0); acc1 = __builtin_amdgcn_mfma_f32_16x16x32_bf16(af, bl[sK][1], acc1, 0, 0, 0); }
; #pragma unroll
;             for (int q = 0; q < 4; ++q) { part[(wave * 16 + 4 * kk + q) * 32 + r16] = acc0[q]; part[(wave * 16 + 4 * kk + q) * 32 + 16 + r16] = acc1[q]; }
.LBB0_1871:
	s_or_b64 exec, exec, s[8:9]
	v_div_scale_f32 v198, s[8:9], v193, v193, s42
	v_rcp_f32_e32 v199, v198
	s_lshl_b64 s[6:7], s[6:7], 11
	v_fma_f32 v200, -v198, v199, 1.0
	v_fmac_f32_e32 v199, v200, v199
	v_div_scale_f32 v200, vcc, s42, v193, s42
	v_mul_f32_e32 v201, v200, v199
	v_fma_f32 v202, -v198, v201, v200
	v_fmac_f32_e32 v201, v202, v199
	v_fma_f32 v198, -v198, v201, v200
	v_div_fmas_f32 v198, v198, v199, v201
	v_div_fixup_f32 v193, v198, v193, s42
	v_fmaak_f32 v196, v196, v193, 0x4b400000
	v_fmaak_f32 v197, v197, v193, 0x4b400000
	v_fmaak_f32 v194, v194, v193, 0x4b400000
	v_fmaak_f32 v195, v195, v193, 0x4b400000
	v_perm_b32 v194, v195, v194, s43
	v_perm_b32 v195, v197, v196, s43
	v_lshl_add_u64 v[198:199], v[136:137], 0, s[6:7]
	v_perm_b32 v194, v194, v195, s44
	global_store_dword v[198:199], v194, off
	v_fmaak_f32 v194, v210, v193, 0x4b400000
	v_fmaak_f32 v195, v211, v193, 0x4b400000
	v_fmaak_f32 v196, v208, v193, 0x4b400000
	v_fmaak_f32 v197, v209, v193, 0x4b400000
	v_perm_b32 v196, v197, v196, s43
	v_perm_b32 v194, v195, v194, s43
	v_perm_b32 v194, v196, v194, s44
	global_store_dword v[198:199], v194, off offset:256
	v_fmaak_f32 v194, v214, v193, 0x4b400000
	v_fmaak_f32 v195, v215, v193, 0x4b400000
	v_fmaak_f32 v196, v212, v193, 0x4b400000
	v_fmaak_f32 v197, v213, v193, 0x4b400000
	v_perm_b32 v196, v197, v196, s43
	v_perm_b32 v194, v195, v194, s43
	v_perm_b32 v194, v196, v194, s44
	global_store_dword v[198:199], v194, off offset:512
	v_fmaak_f32 v194, v218, v193, 0x4b400000
	v_fmaak_f32 v195, v219, v193, 0x4b400000
	v_fmaak_f32 v196, v216, v193, 0x4b400000
	v_fmaak_f32 v197, v217, v193, 0x4b400000
	v_perm_b32 v196, v197, v196, s43
	v_perm_b32 v194, v195, v194, s43
	v_perm_b32 v194, v196, v194, s44
	global_store_dword v[198:199], v194, off offset:768
	v_fmaak_f32 v194, v222, v193, 0x4b400000
	v_fmaak_f32 v195, v223, v193, 0x4b400000
	v_fmaak_f32 v196, v220, v193, 0x4b400000
	v_fmaak_f32 v197, v221, v193, 0x4b400000
	v_perm_b32 v196, v197, v196, s43
	v_perm_b32 v194, v195, v194, s43
	v_perm_b32 v194, v196, v194, s44
	global_store_dword v[198:199], v194, off offset:1024
	v_fmaak_f32 v194, v226, v193, 0x4b400000
	v_fmaak_f32 v195, v227, v193, 0x4b400000
	v_fmaak_f32 v196, v224, v193, 0x4b400000
	v_fmaak_f32 v197, v225, v193, 0x4b400000
	v_fmaak_f32 v132, v132, v193, 0x4b400000
	v_fmaak_f32 v133, v133, v193, 0x4b400000
	v_fmaak_f32 v130, v130, v193, 0x4b400000
	v_fmaak_f32 v131, v131, v193, 0x4b400000
	v_perm_b32 v196, v197, v196, s43
	v_perm_b32 v194, v195, v194, s43
	v_perm_b32 v130, v131, v130, s43
	v_perm_b32 v131, v133, v132, s43
	v_perm_b32 v194, v196, v194, s44
	v_perm_b32 v130, v130, v131, s44
	global_store_dword v[198:199], v194, off offset:1280
	v_fmaak_f32 v194, v230, v193, 0x4b400000
	v_fmaak_f32 v195, v231, v193, 0x4b400000
	v_fmaak_f32 v196, v228, v193, 0x4b400000
	v_fmaak_f32 v197, v229, v193, 0x4b400000
	global_store_dword v[198:199], v130, off offset:1792
	v_add_u32_e32 v130, s36, v1
	v_perm_b32 v196, v197, v196, s43
	v_perm_b32 v194, v195, v194, s43
	v_ashrrev_i32_e32 v131, 31, v130
	v_perm_b32 v194, v196, v194, s44
	v_lshlrev_b64 v[130:131], 12, v[130:131]
	global_store_dword v[198:199], v194, off offset:1536
	v_lshl_add_u64 v[208:209], v[138:139], 0, v[130:131]
	global_load_dwordx4 v[130:133], v[208:209], off
	global_load_dwordx4 v[194:197], v[208:209], off offset:64
	global_load_dwordx4 v[210:213], v[208:209], off offset:128
	global_load_dwordx4 v[214:217], v[208:209], off offset:192
	global_load_dwordx4 v[218:221], v[208:209], off offset:256
	global_load_dwordx4 v[222:225], v[208:209], off offset:320
	global_load_dwordx4 v[226:229], v[208:209], off offset:384
	global_load_dwordx4 v[242:245], v[208:209], off offset:448
	s_waitcnt vmcnt(7)
	v_mfma_f32_16x16x32_bf16 v[198:201], v[130:133], v[122:125], 0
	v_mfma_f32_16x16x32_bf16 v[202:205], v[130:133], v[114:117], 0
	v_mfma_f32_16x16x32_bf16 v[198:201], v[130:133], v[126:129], v[198:201]
	v_mfma_f32_16x16x32_bf16 v[202:205], v[130:133], v[118:121], v[202:205]
	s_waitcnt vmcnt(6)
	v_mfma_f32_16x16x32_bf16 v[198:201], v[194:197], v[106:109], v[198:201]
	v_mfma_f32_16x16x32_bf16 v[202:205], v[194:197], v[98:101], v[202:205]
	v_mfma_f32_16x16x32_bf16 v[198:201], v[194:197], v[110:113], v[198:201]
	v_mfma_f32_16x16x32_bf16 v[202:205], v[194:197], v[102:105], v[202:205]
	s_waitcnt vmcnt(5)
	v_mfma_f32_16x16x32_bf16 v[198:201], v[210:213], v[90:93], v[198:201]
	v_mfma_f32_16x16x32_bf16 v[202:205], v[210:213], v[82:85], v[202:205]
	v_mfma_f32_16x16x32_bf16 v[198:201], v[210:213], v[94:97], v[198:201]
	v_mfma_f32_16x16x32_bf16 v[202:205], v[210:213], v[86:89], v[202:205]
	s_waitcnt vmcnt(4)
	v_mfma_f32_16x16x32_bf16 v[198:201], v[214:217], v[74:77], v[198:201]
	v_mfma_f32_16x16x32_bf16 v[202:205], v[214:217], v[66:69], v[202:205]
	v_mfma_f32_16x16x32_bf16 v[198:201], v[214:217], v[78:81], v[198:201]
	v_mfma_f32_16x16x32_bf16 v[202:205], v[214:217], v[70:73], v[202:205]
	s_waitcnt vmcnt(3)
	v_mfma_f32_16x16x32_bf16 v[198:201], v[218:221], v[58:61], v[198:201]
	v_mfma_f32_16x16x32_bf16 v[202:205], v[218:221], v[50:53], v[202:205]
	v_mfma_f32_16x16x32_bf16 v[198:201], v[218:221], v[62:65], v[198:201]
	v_mfma_f32_16x16x32_bf16 v[202:205], v[218:221], v[54:57], v[202:205]
	s_waitcnt vmcnt(2)
	v_mfma_f32_16x16x32_bf16 v[198:201], v[222:225], v[42:45], v[198:201]
	v_mfma_f32_16x16x32_bf16 v[202:205], v[222:225], v[34:37], v[202:205]
	v_mfma_f32_16x16x32_bf16 v[198:201], v[222:225], v[46:49], v[198:201]
	v_mfma_f32_16x16x32_bf16 v[202:205], v[222:225], v[38:41], v[202:205]
	s_waitcnt vmcnt(1)
	v_mfma_f32_16x16x32_bf16 v[198:201], v[226:229], v[26:29], v[198:201]
	v_mfma_f32_16x16x32_bf16 v[202:205], v[226:229], v[18:21], v[202:205]
	v_mfma_f32_16x16x32_bf16 v[198:201], v[226:229], v[30:33], v[198:201]
	v_mfma_f32_16x16x32_bf16 v[202:205], v[226:229], v[22:25], v[202:205]
	s_waitcnt vmcnt(0)
	v_mfma_f32_16x16x32_bf16 v[198:201], v[242:245], v[6:9], v[198:201]
	v_mfma_f32_16x16x32_bf16 v[202:205], v[242:245], v[2:5], v[202:205]
	v_mfma_f32_16x16x32_bf16 v[198:201], v[242:245], v[14:17], v[198:201]
	v_mfma_f32_16x16x32_bf16 v[202:205], v[242:245], v[10:13], v[202:205]
	s_nop 7
	ds_write2_b32 v239, v198, v202 offset1:16
	ds_write2_b32 v239, v199, v203 offset0:32 offset1:48
	ds_write2_b32 v239, v200, v204 offset0:64 offset1:80
	ds_write2_b32 v239, v201, v205 offset0:96 offset1:112
	s_waitcnt lgkmcnt(0)
	s_barrier
; __global__ void __launch_bounds__(NWAVES * 64, 2) fwd_kernel(Args a_unused) {
;     ...
;             { const int row = tid >> 5, e = tid & 31; float s = 0.f;
; #pragma unroll
;               for (int w = 0; w < 8; ++w) s += part[(w * 16 + row) * 32 + e];
;               float val = rsd[row] * s + cvec[e];
;               float tv[4]; int ti[4];
; #pragma unroll
;               for (int j = 0; j < 4; ++j) { float bv = val; int bi = e;
; #pragma unroll
;                   for (int off = 16; off >= 1; off >>= 1) { const float ov = __shfl_xor(bv, off); const int oi = __shfl_xor(bi, off); if (ov > bv || (ov == bv && oi < bi)) { bv = ov; bi = oi; } }
;                   tv[j] = bv; ti[j] = bi; if (e == bi) val = -INFINITY; }
	global_load_dword v131, v[140:141], off
	ds_read2st64_b32 v[132:133], v236 offset1:8
	ds_read2st64_b32 v[194:195], v236 offset0:16 offset1:24
	ds_read2st64_b32 v[196:197], v236 offset0:32 offset1:40
	ds_read2st64_b32 v[198:199], v236 offset0:48 offset1:56
	ds_read_b32 v130, v237 offset:16384
	s_waitcnt lgkmcnt(4)
	v_add_f32_e32 v132, 0, v132
	v_add_f32_e32 v132, v132, v133
	s_waitcnt lgkmcnt(3)
	v_add_f32_e32 v132, v132, v194
	v_add_f32_e32 v132, v132, v195
	s_waitcnt lgkmcnt(2)
	v_add_f32_e32 v132, v132, v196
	v_add_f32_e32 v132, v132, v197
	s_waitcnt lgkmcnt(1)
	v_add_f32_e32 v132, v132, v198
	v_add_f32_e32 v132, v132, v199
	s_waitcnt vmcnt(0) lgkmcnt(0)
	v_fmac_f32_e32 v131, v132, v130
	v_mov_b32_e32 v196, v131
	v_mov_b32_e32 v197, v196
	v_mov_b32_e32 v198, v235
	s_nop 1
	v_mov_b32_dpp v194, v197 quad_perm:[1,0,3,2] row_mask:0xf bank_mask:0xf
	v_mov_b32_dpp v195, v198 quad_perm:[1,0,3,2] row_mask:0xf bank_mask:0xf
	v_cmp_gt_f32_e32 vcc, v194, v197
	v_cmp_eq_f32_e64 s[12:13], v194, v197
	v_cmp_lt_i32_e64 s[26:27], v195, v198
	s_and_b64 s[12:13], s[12:13], s[26:27]
	s_or_b64 vcc, vcc, s[12:13]
	v_cndmask_b32_e32 v197, v197, v194, vcc
	v_cndmask_b32_e32 v198, v198, v195, vcc
	s_nop 1
	v_mov_b32_dpp v194, v197 quad_perm:[2,3,0,1] row_mask:0xf bank_mask:0xf
	v_mov_b32_dpp v195, v198 quad_perm:[2,3,0,1] row_mask:0xf bank_mask:0xf
	v_cmp_gt_f32_e32 vcc, v194, v197
	v_cmp_eq_f32_e64 s[12:13], v194, v197
	v_cmp_lt_i32_e64 s[26:27], v195, v198
	s_and_b64 s[12:13], s[12:13], s[26:27]
	s_or_b64 vcc, vcc, s[12:13]
	v_cndmask_b32_e32 v197, v197, v194, vcc
	v_cndmask_b32_e32 v198, v198, v195, vcc
	s_nop 1
	v_mov_b32_dpp v194, v197 row_half_mirror row_mask:0xf bank_mask:0xf
	v_mov_b32_dpp v195, v198 row_half_mirror row_mask:0xf bank_mask:0xf
	v_cmp_gt_f32_e32 vcc, v194, v197
	v_cmp_eq_f32_e64 s[12:13], v194, v197
	v_cmp_lt_i32_e64 s[26:27], v195, v198
	s_and_b64 s[12:13], s[12:13], s[26:27]
	s_or_b64 vcc, vcc, s[12:13]
	v_cndmask_b32_e32 v197, v197, v194, vcc
	v_cndmask_b32_e32 v198, v198, v195, vcc
	s_nop 1
	v_mov_b32_dpp v194, v197 row_mirror row_mask:0xf bank_mask:0xf
	v_mov_b32_dpp v195, v198 row_mirror row_mask:0xf bank_mask:0xf
	v_cmp_gt_f32_e32 vcc, v194, v197
	v_cmp_eq_f32_e64 s[12:13], v194, v197
	v_cmp_lt_i32_e64 s[26:27], v195, v198
	s_and_b64 s[12:13], s[12:13], s[26:27]
	s_or_b64 vcc, vcc, s[12:13]
	v_cndmask_b32_e32 v197, v197, v194, vcc
	v_cndmask_b32_e32 v198, v198, v195, vcc
	v_mov_b32_e32 v194, v197
	v_mov_b32_e32 v195, v198
	s_nop 1
	v_permlane16_swap_b32 v197, v194
	v_permlane16_swap_b32 v198, v195
	v_cmp_gt_f32_e32 vcc, v194, v197
	v_cmp_eq_f32_e64 s[12:13], v194, v197
	v_cmp_lt_i32_e64 s[26:27], v195, v198
	s_and_b64 s[12:13], s[12:13], s[26:27]
	s_or_b64 vcc, vcc, s[12:13]
	v_cndmask_b32_e32 v197, v197, v194, vcc
	v_cndmask_b32_e32 v198, v198, v195, vcc
	v_mov_b32_e32 v130, v197
	v_cmp_eq_u32_e64 s[6:7], v235, v198
	s_nop 1
	v_cndmask_b32_e64 v196, v196, v241, s[6:7]
	v_mov_b32_e32 v197, v196
	v_mov_b32_e32 v198, v235
	s_nop 1
	v_mov_b32_dpp v194, v197 quad_perm:[1,0,3,2] row_mask:0xf bank_mask:0xf
	v_mov_b32_dpp v195, v198 quad_perm:[1,0,3,2] row_mask:0xf bank_mask:0xf
	v_cmp_gt_f32_e32 vcc, v194, v197
	v_cmp_eq_f32_e64 s[12:13], v194, v197
	v_cmp_lt_i32_e64 s[26:27], v195, v198
	s_and_b64 s[12:13], s[12:13], s[26:27]
	s_or_b64 vcc, vcc, s[12:13]
	v_cndmask_b32_e32 v197, v197, v194, vcc
	v_cndmask_b32_e32 v198, v198, v195, vcc
	s_nop 1
	v_mov_b32_dpp v194, v197 quad_perm:[2,3,0,1] row_mask:0xf bank_mask:0xf
	v_mov_b32_dpp v195, v198 quad_perm:[2,3,0,1] row_mask:0xf bank_mask:0xf
	v_cmp_gt_f32_e32 vcc, v194, v197
	v_cmp_eq_f32_e64 s[12:13], v194, v197
	v_cmp_lt_i32_e64 s[26:27], v195, v198
	s_and_b64 s[12:13], s[12:13], s[26:27]
	s_or_b64 vcc, vcc, s[12:13]
	v_cndmask_b32_e32 v197, v197, v194, vcc
	v_cndmask_b32_e32 v198, v198, v195, vcc
	s_nop 1
	v_mov_b32_dpp v194, v197 row_half_mirror row_mask:0xf bank_mask:0xf
	v_mov_b32_dpp v195, v198 row_half_mirror row_mask:0xf bank_mask:0xf
	v_cmp_gt_f32_e32 vcc, v194, v197
	v_cmp_eq_f32_e64 s[12:13], v194, v197
	v_cmp_lt_i32_e64 s[26:27], v195, v198
	s_and_b64 s[12:13], s[12:13], s[26:27]
	s_or_b64 vcc, vcc, s[12:13]
	v_cndmask_b32_e32 v197, v197, v194, vcc
	v_cndmask_b32_e32 v198, v198, v195, vcc
	s_nop 1
	v_mov_b32_dpp v194, v197 row_mirror row_mask:0xf bank_mask:0xf
	v_mov_b32_dpp v195, v198 row_mirror row_mask:0xf bank_mask:0xf
	v_cmp_gt_f32_e32 vcc, v194, v197
	v_cmp_eq_f32_e64 s[12:13], v194, v197
	v_cmp_lt_i32_e64 s[26:27], v195, v198
	s_and_b64 s[12:13], s[12:13], s[26:27]
	s_or_b64 vcc, vcc, s[12:13]
	v_cndmask_b32_e32 v197, v197, v194, vcc
	v_cndmask_b32_e32 v198, v198, v195, vcc
	v_mov_b32_e32 v194, v197
	v_mov_b32_e32 v195, v198
	s_nop 1
	v_permlane16_swap_b32 v197, v194
	v_permlane16_swap_b32 v198, v195
	v_cmp_gt_f32_e32 vcc, v194, v197
	v_cmp_eq_f32_e64 s[12:13], v194, v197
	v_cmp_lt_i32_e64 s[26:27], v195, v198
	s_and_b64 s[12:13], s[12:13], s[26:27]
	s_or_b64 vcc, vcc, s[12:13]
	v_cndmask_b32_e32 v197, v197, v194, vcc
	v_cndmask_b32_e32 v198, v198, v195, vcc
	v_mov_b32_e32 v131, v197
	v_cmp_eq_u32_e64 s[8:9], v235, v198
	s_nop 1
	v_cndmask_b32_e64 v196, v196, v241, s[8:9]
	v_mov_b32_e32 v197, v196
	v_mov_b32_e32 v198, v235
	s_nop 1
	v_mov_b32_dpp v194, v197 quad_perm:[1,0,3,2] row_mask:0xf bank_mask:0xf
	v_mov_b32_dpp v195, v198 quad_perm:[1,0,3,2] row_mask:0xf bank_mask:0xf
	v_cmp_gt_f32_e32 vcc, v194, v197
	v_cmp_eq_f32_e64 s[12:13], v194, v197
	v_cmp_lt_i32_e64 s[26:27], v195, v198
	s_and_b64 s[12:13], s[12:13], s[26:27]
	s_or_b64 vcc, vcc, s[12:13]
	v_cndmask_b32_e32 v197, v197, v194, vcc
	v_cndmask_b32_e32 v198, v198, v195, vcc
	s_nop 1
; __global__ void __launch_bounds__(NWAVES * 64, 2) fwd_kernel(Args a_unused) {
;     ...
;               for (int j = 0; j < 4; ++j) { float bv = val; int bi = e;
; #pragma unroll
;                   for (int off = 16; off >= 1; off >>= 1) { const float ov = __shfl_xor(bv, off); const int oi = __shfl_xor(bi, off); if (ov > bv || (ov == bv && oi < bi)) { bv = ov; bi = oi; } }
;                   tv[j] = bv; ti[j] = bi; if (e == bi) val = -INFINITY; }
;               const float e1 = __expf(tv[1] - tv[0]), e2 = __expf(tv[2] - tv[0]), e3 = __expf(tv[3] - tv[0]), inv = 1.0f / (1.0f + e1 + e2 + e3);
;               const float gt[4] = {inv, e1 * inv, e2 * inv, e3 * inv};
; #pragma unroll
;               for (int j = 0; j < 4; ++j) if (e == ti[j]) { const int ai = (row0 + row) * 4 + j; const unsigned rk = atomicAdd(ctl + CW_CNT + 16 * e, 1u);
;                   rt_e[ai] = e; rt_g[ai] = gt[j]; rt_r[ai] = (int)rk; } }
	v_mov_b32_dpp v194, v197 quad_perm:[2,3,0,1] row_mask:0xf bank_mask:0xf
	v_mov_b32_dpp v195, v198 quad_perm:[2,3,0,1] row_mask:0xf bank_mask:0xf
	v_cmp_gt_f32_e32 vcc, v194, v197
	v_cmp_eq_f32_e64 s[12:13], v194, v197
	v_cmp_lt_i32_e64 s[26:27], v195, v198
	s_and_b64 s[12:13], s[12:13], s[26:27]
	s_or_b64 vcc, vcc, s[12:13]
	v_cndmask_b32_e32 v197, v197, v194, vcc
	v_cndmask_b32_e32 v198, v198, v195, vcc
	s_nop 1
	v_mov_b32_dpp v194, v197 row_half_mirror row_mask:0xf bank_mask:0xf
	v_mov_b32_dpp v195, v198 row_half_mirror row_mask:0xf bank_mask:0xf
	v_cmp_gt_f32_e32 vcc, v194, v197
	v_cmp_eq_f32_e64 s[12:13], v194, v197
	v_cmp_lt_i32_e64 s[26:27], v195, v198
	s_and_b64 s[12:13], s[12:13], s[26:27]
	s_or_b64 vcc, vcc, s[12:13]
	v_cndmask_b32_e32 v197, v197, v194, vcc
	v_cndmask_b32_e32 v198, v198, v195, vcc
	s_nop 1
	v_mov_b32_dpp v194, v197 row_mirror row_mask:0xf bank_mask:0xf
	v_mov_b32_dpp v195, v198 row_mirror row_mask:0xf bank_mask:0xf
	v_cmp_gt_f32_e32 vcc, v194, v197
	v_cmp_eq_f32_e64 s[12:13], v194, v197
	v_cmp_lt_i32_e64 s[26:27], v195, v198
	s_and_b64 s[12:13], s[12:13], s[26:27]
	s_or_b64 vcc, vcc, s[12:13]
	v_cndmask_b32_e32 v197, v197, v194, vcc
	v_cndmask_b32_e32 v198, v198, v195, vcc
	v_mov_b32_e32 v194, v197
	v_mov_b32_e32 v195, v198
	s_nop 1
	v_permlane16_swap_b32 v197, v194
	v_permlane16_swap_b32 v198, v195
	v_cmp_gt_f32_e32 vcc, v194, v197
	v_cmp_eq_f32_e64 s[12:13], v194, v197
	v_cmp_lt_i32_e64 s[26:27], v195, v198
	s_and_b64 s[12:13], s[12:13], s[26:27]
	s_or_b64 vcc, vcc, s[12:13]
	v_cndmask_b32_e32 v197, v197, v194, vcc
	v_cndmask_b32_e32 v198, v198, v195, vcc
	v_mov_b32_e32 v132, v197
	v_cmp_eq_u32_e64 s[10:11], v235, v198
	s_nop 1
	v_cndmask_b32_e64 v196, v196, v241, s[10:11]
	v_mov_b32_e32 v197, v196
	v_mov_b32_e32 v198, v235
	s_nop 1
	v_mov_b32_dpp v194, v197 quad_perm:[1,0,3,2] row_mask:0xf bank_mask:0xf
	v_mov_b32_dpp v195, v198 quad_perm:[1,0,3,2] row_mask:0xf bank_mask:0xf
	v_cmp_gt_f32_e32 vcc, v194, v197
	v_cmp_eq_f32_e64 s[12:13], v194, v197
	v_cmp_lt_i32_e64 s[26:27], v195, v198
	s_and_b64 s[12:13], s[12:13], s[26:27]
	s_or_b64 vcc, vcc, s[12:13]
	v_cndmask_b32_e32 v197, v197, v194, vcc
	v_cndmask_b32_e32 v198, v198, v195, vcc
	s_nop 1
	v_mov_b32_dpp v194, v197 quad_perm:[2,3,0,1] row_mask:0xf bank_mask:0xf
	v_mov_b32_dpp v195, v198 quad_perm:[2,3,0,1] row_mask:0xf bank_mask:0xf
	v_cmp_gt_f32_e32 vcc, v194, v197
	v_cmp_eq_f32_e64 s[12:13], v194, v197
	v_cmp_lt_i32_e64 s[26:27], v195, v198
	s_and_b64 s[12:13], s[12:13], s[26:27]
	s_or_b64 vcc, vcc, s[12:13]
	v_cndmask_b32_e32 v197, v197, v194, vcc
	v_cndmask_b32_e32 v198, v198, v195, vcc
	s_nop 1
	v_mov_b32_dpp v194, v197 row_half_mirror row_mask:0xf bank_mask:0xf
	v_mov_b32_dpp v195, v198 row_half_mirror row_mask:0xf bank_mask:0xf
	v_cmp_gt_f32_e32 vcc, v194, v197
	v_cmp_eq_f32_e64 s[12:13], v194, v197
	v_cmp_lt_i32_e64 s[26:27], v195, v198
	s_and_b64 s[12:13], s[12:13], s[26:27]
	s_or_b64 vcc, vcc, s[12:13]
	v_cndmask_b32_e32 v197, v197, v194, vcc
	v_cndmask_b32_e32 v198, v198, v195, vcc
	s_nop 1
	v_mov_b32_dpp v194, v197 row_mirror row_mask:0xf bank_mask:0xf
	v_mov_b32_dpp v195, v198 row_mirror row_mask:0xf bank_mask:0xf
	v_cmp_gt_f32_e32 vcc, v194, v197
	v_cmp_eq_f32_e64 s[12:13], v194, v197
	v_cmp_lt_i32_e64 s[26:27], v195, v198
	s_and_b64 s[12:13], s[12:13], s[26:27]
	s_or_b64 vcc, vcc, s[12:13]
	v_cndmask_b32_e32 v197, v197, v194, vcc
	v_cndmask_b32_e32 v198, v198, v195, vcc
	v_mov_b32_e32 v194, v197
	v_mov_b32_e32 v195, v198
	s_nop 1
	v_permlane16_swap_b32 v197, v194
	v_permlane16_swap_b32 v198, v195
	v_cmp_gt_f32_e32 vcc, v194, v197
	v_cmp_eq_f32_e64 s[12:13], v194, v197
	v_cmp_lt_i32_e64 s[26:27], v195, v198
	s_and_b64 s[12:13], s[12:13], s[26:27]
	s_or_b64 vcc, vcc, s[12:13]
	v_cndmask_b32_e32 v197, v197, v194, vcc
	v_cndmask_b32_e32 v198, v198, v195, vcc
	v_mov_b32_e32 v193, v197
	v_mov_b32_e32 v133, v198
	v_sub_f32_e32 v131, v131, v130
	v_mul_f32_e32 v131, 0x3fb8aa3b, v131
	v_exp_f32_e32 v194, v131
	v_sub_f32_e32 v131, v132, v130
	v_mul_f32_e32 v131, 0x3fb8aa3b, v131
	v_sub_f32_e32 v130, v193, v130
	v_exp_f32_e32 v132, v131
	v_mul_f32_e32 v130, 0x3fb8aa3b, v130
	v_exp_f32_e32 v130, v130
	v_add_f32_e32 v131, 1.0, v194
	v_add_f32_e32 v131, v131, v132
	v_add_f32_e32 v131, v131, v130
	v_div_scale_f32 v193, s[12:13], v131, v131, 1.0
	s_waitcnt lgkmcnt(0)
	v_rcp_f32_e32 v195, v193
	s_nop 0
	v_fma_f32 v196, -v193, v195, 1.0
	v_fmac_f32_e32 v195, v196, v195
	v_div_scale_f32 v196, vcc, 1.0, v131, 1.0
	v_mul_f32_e32 v197, v196, v195
	v_fma_f32 v198, -v193, v197, v196
	v_fmac_f32_e32 v197, v198, v195
	v_fma_f32 v193, -v193, v197, v196
	v_div_fmas_f32 v193, v193, v195, v197
	v_div_fixup_f32 v131, v193, v131, 1.0
	v_mul_f32_e32 v198, v194, v131
	v_mul_f32_e32 v132, v132, v131
	v_mul_f32_e32 v195, v130, v131
	v_cmp_eq_u32_e64 s[12:13], v235, v133
	v_add_u32_e32 v196, -1, v192
	v_add_u32_e32 v197, -2, v192
	v_add_u32_e32 v199, -3, v192
	v_cndmask_b32_e64 v195, v195, v132, s[10:11]
	v_cndmask_b32_e64 v130, v192, v196, s[10:11]
	v_cndmask_b32_e64 v195, v195, v198, s[8:9]
	v_cndmask_b32_e64 v130, v130, v197, s[8:9]
	v_cndmask_b32_e64 v195, v195, v131, s[6:7]
	v_cndmask_b32_e64 v130, v130, v199, s[6:7]
	s_or_b64 s[8:9], s[6:7], s[8:9]
	s_or_b64 s[10:11], s[10:11], s[12:13]
	s_or_b64 s[8:9], s[8:9], s[10:11]
	s_and_saveexec_b64 s[6:7], s[8:9]
	s_cbranch_execz .LBB0_1862
	global_atomic_add v193, v[142:143], v240, off sc0
	v_ashrrev_i32_e32 v131, 31, v130
	v_lshlrev_b64 v[130:131], 2, v[130:131]
	v_lshl_add_u64 v[132:133], s[20:21], 0, v[130:131]
	v_lshl_add_u64 v[196:197], s[22:23], 0, v[130:131]
	v_lshl_add_u64 v[198:199], s[24:25], 0, v[130:131]
	global_store_dword v[132:133], v235, off
	global_store_dword v[196:197], v195, off
	s_waitcnt vmcnt(2)
	global_store_dword v[198:199], v193, off
	s_branch .LBB0_1862
